# v048 + item-0 first weight chunks (W0/W1, 6 loads) issued in audio pre-phase at kt=4 instead of at its end; later vmcnt waits +6
# baseline (speedup 1.0000x reference)
.LBB3_92:
	v_add_co_u32_e32 v58, vcc, 0x7000, v158
	s_nop 1
	v_addc_co_u32_e32 v59, vcc, 0, v159, vcc
	s_waitcnt lgkmcnt(3)
	global_load_dwordx4 v[78:81], v[58:59], off
	global_load_dwordx4 v[74:77], v[58:59], off offset:1024
	global_load_dwordx4 v[70:73], v[58:59], off offset:2048
	s_nop 0
	global_load_dwordx4 v[58:61], v[58:59], off offset:3072
	s_mul_i32 s44, s16, 0x180000
	s_add_u32 s44, s6, s44
	s_addc_u32 s45, s7, 0
	v_lshlrev_b32_e64 v212, 6, s23
	v_lshlrev_b32_e64 v213, 6, s3
	v_or_b32_e32 v214, 0x400, v212
	v_or_b32_e32 v215, 4, v160
	v_or_b32_e32 v216, v212, v160
	v_lshl_or_b32 v216, v216, 10, v202
	global_load_dwordx4 v[190:193], v216, s[44:45]
	v_or_b32_e32 v216, v213, v160
	v_lshl_or_b32 v216, v216, 10, v202
	global_load_dwordx4 v[194:197], v216, s[44:45]
	v_or_b32_e32 v216, v214, v160
	v_lshl_or_b32 v216, v216, 10, v202
	global_load_dwordx4 v[198:201], v216, s[44:45]
	v_or_b32_e32 v216, v215, v212
	v_lshl_or_b32 v216, v216, 10, v202
	global_load_dwordx4 v[174:177], v216, s[44:45]
	v_or_b32_e32 v216, v213, v215
	v_lshl_or_b32 v216, v216, 10, v202
	global_load_dwordx4 v[182:185], v216, s[44:45]
	v_or_b32_e32 v216, v214, v215
	v_lshl_or_b32 v216, v216, 10, v202
	global_load_dwordx4 v[186:189], v216, s[44:45]
	ds_read_b128 v[142:145], v161 offset:50176
	ds_read_b128 v[134:137], v161 offset:54272
	ds_read_b128 v[130:133], v161 offset:58368
	s_waitcnt vmcnt(19)
	ds_write_b128 v165, v[114:117]
	s_waitcnt vmcnt(18)
	ds_write_b128 v165, v[118:121] offset:8192
	s_waitcnt vmcnt(17)
	ds_write_b128 v165, v[122:125] offset:16384
	s_waitcnt lgkmcnt(6)
	v_mfma_f32_32x32x16_bf16 v[18:33], v[138:141], v[102:105], v[18:33]
	s_cmp_lg_u64 s[4:5], 0
	s_cbranch_scc0 .LBB3_94
	v_mfma_f32_32x32x16_bf16 v[2:17], v[102:105], v[106:109], v[2:17]
	v_mfma_f32_32x32x16_bf16 v[34:49], v[102:105], v[98:101], v[34:49]
	s_branch .LBB3_96

.LBB3_108:
	s_waitcnt vmcnt(12)
	ds_write_b128 v165, v[94:97] offset:24576
	s_waitcnt vmcnt(11)
	ds_write_b128 v165, v[110:113] offset:32768
	s_waitcnt vmcnt(10)
	ds_write_b128 v165, v[126:129] offset:40960
	s_waitcnt lgkmcnt(7)
	ds_read_b128 v[106:109], v161 offset:1024
	ds_read_b128 v[94:97], v161 offset:5120
	s_waitcnt lgkmcnt(8)
	ds_read_b128 v[82:85], v161 offset:9216
	s_waitcnt lgkmcnt(6)
	v_mfma_f32_32x32x16_bf16 v[18:33], v[102:105], v[90:93], v[18:33]
	s_cmp_lg_u64 s[4:5], 0
	s_cbranch_scc0 .LBB3_110
	v_mfma_f32_32x32x16_bf16 v[2:17], v[90:93], v[98:101], v[2:17]
	v_mfma_f32_32x32x16_bf16 v[34:49], v[90:93], v[62:65], v[34:49]
	s_branch .LBB3_112

.LBB3_124:
	s_waitcnt lgkmcnt(4)
	ds_read_b128 v[82:85], v161 offset:29696
	ds_read_b128 v[86:89], v161 offset:25600
	s_waitcnt lgkmcnt(5)
	ds_read_b128 v[62:65], v161 offset:33792
	s_waitcnt vmcnt(9) lgkmcnt(3)
	v_mfma_f32_32x32x16_bf16 v[18:33], v[90:93], v[78:81], v[18:33]
	s_cmp_lg_u64 s[4:5], 0
	s_cbranch_scc0 .LBB3_126
	v_mfma_f32_32x32x16_bf16 v[2:17], v[78:81], v[66:69], v[2:17]
	v_mfma_f32_32x32x16_bf16 v[34:49], v[78:81], v[54:57], v[34:49]
	s_branch .LBB3_128

.LBB3_128:
	s_waitcnt lgkmcnt(3)
	ds_read_b128 v[54:57], v161 offset:30720
	ds_read_b128 v[78:81], v161 offset:26624
	ds_read_b128 v[50:53], v161 offset:34816
	s_waitcnt vmcnt(8) lgkmcnt(3)
	v_mfma_f32_32x32x16_bf16 v[18:33], v[86:89], v[74:77], v[18:33]
	s_cmp_lg_u64 s[4:5], 0
	s_cbranch_scc0 .LBB3_130
	v_mfma_f32_32x32x16_bf16 v[2:17], v[74:77], v[82:85], v[2:17]
	v_mfma_f32_32x32x16_bf16 v[34:49], v[74:77], v[62:65], v[34:49]
	s_branch .LBB3_132

.LBB3_132:
	s_waitcnt lgkmcnt(3)
	s_barrier
	ds_read_b128 v[66:69], v161 offset:31744
	ds_read_b128 v[74:77], v161 offset:27648
	s_waitcnt lgkmcnt(5)
	ds_read_b128 v[62:65], v161 offset:35840
	s_waitcnt vmcnt(7) lgkmcnt(3)
	v_mfma_f32_32x32x16_bf16 v[18:33], v[78:81], v[70:73], v[18:33]
	s_cmp_lg_u64 s[4:5], 0
	s_cbranch_scc0 .LBB3_134
	v_mfma_f32_32x32x16_bf16 v[2:17], v[70:73], v[54:57], v[2:17]
	v_mfma_f32_32x32x16_bf16 v[34:49], v[70:73], v[50:53], v[34:49]
	s_branch .LBB3_136

.LBB3_136:
	s_load_dwordx2 s[8:9], s[0:1], 0x20
	s_waitcnt vmcnt(6) lgkmcnt(0)
	s_nop 1
	v_mfma_f32_32x32x16_bf16 v[18:33], v[74:77], v[58:61], v[18:33]
	s_cmp_lg_u64 s[4:5], 0
	s_cbranch_scc0 .LBB3_138
	v_mfma_f32_32x32x16_bf16 v[2:17], v[58:61], v[66:69], v[2:17]
	v_mfma_f32_32x32x16_bf16 v[34:49], v[58:61], v[62:65], v[34:49]
	s_branch .LBB3_140

.LBB3_140:
	s_load_dwordx2 s[4:5], s[0:1], 0x30
	s_load_dwordx2 s[10:11], s[0:1], 0x0
	s_load_dwordx2 s[12:13], s[0:1], 0x28
	s_load_dwordx2 s[14:15], s[0:1], 0x38
	s_lshr_b32 s0, s2, 6
	s_add_i32 s0, s17, s0
	v_lshl_or_b32 v206, s0, 3, v1
	s_mul_i32 s0, s16, 0x180000
	v_mov_b32_e32 v207, 0
	s_add_u32 s0, s6, s0
	v_lshlrev_b32_e64 v58, 6, s23
	v_mov_b32_e32 v203, v207
	s_addc_u32 s1, s7, 0
	v_or_b32_e32 v54, v58, v160
	v_lshlrev_b32_e64 v59, 6, s3
	v_lshlrev_b64 v[50:51], 15, v[206:207]
	v_lshl_add_u64 v[52:53], s[0:1], 0, v[202:203]
	v_lshlrev_b32_e32 v206, 10, v54
	v_or_b32_e32 v56, v59, v160
	v_lshl_add_u64 v[54:55], v[52:53], 0, v[206:207]
	v_lshlrev_b32_e32 v206, 10, v56
	v_or_b32_e32 v60, 0x400, v58
	s_waitcnt lgkmcnt(0)
	s_barrier
	v_lshl_add_u64 v[56:57], v[52:53], 0, v[206:207]
	v_or_b32_e32 v54, v60, v160
	v_or_b32_e32 v61, 4, v160
	v_lshlrev_b32_e32 v206, 10, v54
	v_or_b32_e32 v56, v61, v58
	v_lshl_add_u64 v[54:55], v[52:53], 0, v[206:207]
	v_lshlrev_b32_e32 v206, 10, v56
	v_lshl_add_u64 v[56:57], v[52:53], 0, v[206:207]
	v_or_b32_e32 v54, v59, v61
	v_lshlrev_b32_e32 v206, 10, v54
	v_or_b32_e32 v56, v60, v61
	v_lshl_add_u64 v[50:51], s[10:11], 0, v[50:51]
	v_lshl_add_u64 v[54:55], v[52:53], 0, v[206:207]
	v_lshlrev_b32_e32 v206, 10, v56
	v_lshl_add_u64 v[50:51], v[50:51], 0, v[202:203]
	v_lshl_add_u64 v[52:53], v[52:53], 0, v[206:207]
	s_movk_i32 s2, 0x1000
	global_load_dwordx4 v[170:173], v[50:51], off
	global_load_dwordx4 v[162:165], v[50:51], off offset:1024
	global_load_dwordx4 v[154:157], v[50:51], off offset:2048
	global_load_dwordx4 v[146:149], v[50:51], off offset:3072
	v_add_co_u32_e32 v52, vcc, s2, v50
	s_movk_i32 s26, 0x2000
	s_nop 0
	v_addc_co_u32_e32 v53, vcc, 0, v51, vcc
	v_add_co_u32_e32 v50, vcc, s26, v50
	v_lshlrev_b32_e32 v1, 1, v1
	s_nop 0
	v_addc_co_u32_e32 v51, vcc, 0, v51, vcc
	global_load_dwordx4 v[166:169], v[52:53], off offset:1024
	global_load_dwordx4 v[158:161], v[52:53], off offset:2048
	global_load_dwordx4 v[178:181], v[50:51], off offset:-4096
	global_load_dwordx4 v[150:153], v[52:53], off offset:3072
	global_load_dwordx4 v[142:145], v[50:51], off
	global_load_dwordx4 v[138:141], v[50:51], off offset:1024
	global_load_dwordx4 v[134:137], v[50:51], off offset:2048
	global_load_dwordx4 v[130:133], v[50:51], off offset:3072
	v_mul_u32_u24_e32 v50, 0x6000, v205
	v_mul_u32_u24_e32 v52, 12, v208
	v_or_b32_e32 v50, v50, v202
	v_lshlrev_b32_e32 v51, 2, v204
	v_and_b32_e32 v52, 8, v52
	v_and_b32_e32 v1, 2, v1
	v_add_u32_e32 v50, 0x12000, v50
	v_or3_b32 v1, v1, v52, v51
	v_cvt_pk_bf16_f32 v18, v18, v19
	v_cvt_pk_bf16_f32 v19, v20, v21
	v_cvt_pk_bf16_f32 v20, v22, v23
	v_cvt_pk_bf16_f32 v21, v24, v25
	v_lshl_add_u32 v1, v1, 10, v50
	ds_write_b128 v1, v[18:21]
	v_cvt_pk_bf16_f32 v18, v26, v27
	v_cvt_pk_bf16_f32 v19, v28, v29
	v_cvt_pk_bf16_f32 v20, v30, v31
	v_cvt_pk_bf16_f32 v21, v32, v33
	ds_write_b128 v1, v[18:21] offset:1024
	v_mad_u32_u24 v1, v208, 3, 1
	v_lshlrev_b32_e32 v18, 2, v1
	v_lshlrev_b32_e32 v1, 1, v1
	v_and_b32_e32 v18, 24, v18
	v_and_b32_e32 v1, 2, v1
	v_or3_b32 v1, v1, v18, v51
	v_cvt_pk_bf16_f32 v2, v2, v3
	v_cvt_pk_bf16_f32 v3, v4, v5
	v_cvt_pk_bf16_f32 v4, v6, v7
	v_cvt_pk_bf16_f32 v5, v8, v9
	v_lshl_add_u32 v1, v1, 10, v50
	ds_write_b128 v1, v[2:5]
	v_cvt_pk_bf16_f32 v2, v10, v11
	v_cvt_pk_bf16_f32 v3, v12, v13
	v_cvt_pk_bf16_f32 v4, v14, v15
	v_cvt_pk_bf16_f32 v5, v16, v17
	ds_write_b128 v1, v[2:5] offset:1024
	v_mad_u32_u24 v1, v208, 3, 2
	v_lshlrev_b32_e32 v2, 2, v1
	v_lshlrev_b32_e32 v1, 1, v1
	s_lshl_b32 s2, s17, 3
	v_and_b32_e32 v2, 24, v2
	v_and_b32_e32 v1, 2, v1
	s_add_i32 s2, s22, s2
	v_or3_b32 v1, v1, v2, v51
	s_add_i32 s2, s2, 32
	v_cvt_pk_bf16_f32 v2, v34, v35
	v_cvt_pk_bf16_f32 v3, v36, v37
	v_cvt_pk_bf16_f32 v4, v38, v39
	v_cvt_pk_bf16_f32 v5, v40, v41
	v_lshl_add_u32 v1, v1, 10, v50
	s_mov_b32 s3, 0
	s_lshl_b32 s6, s23, 6
	s_and_b32 s28, s2, 0x7ffffff8
	s_lshl_b32 s2, s16, 9
	s_movk_i32 s27, 0x6000
	ds_write_b128 v1, v[2:5]
	v_cvt_pk_bf16_f32 v2, v42, v43
	v_cvt_pk_bf16_f32 v3, v44, v45
	v_cvt_pk_bf16_f32 v4, v46, v47
	v_cvt_pk_bf16_f32 v5, v48, v49
	s_mov_b32 s7, s3
	s_or_b32 s16, s2, s6
	s_mov_b32 s17, s3
	s_mov_b64 s[20:21], -1
	s_movk_i32 s29, 0x3000
	s_movk_i32 s30, 0x4000
	s_movk_i32 s31, 0x5000
	s_movk_i32 s33, 0x7000
	s_mov_b32 s34, 0x8000
	s_mov_b32 s35, 0xa000
	s_mov_b32 s36, 0xc000
	s_mov_b32 s37, 0xe000
	s_mov_b32 s38, 0xf149f2ca
	s_mov_b32 s39, 0x9000
	s_mov_b32 s40, 0xb000
	s_mov_b32 s41, 0
	ds_write_b128 v1, v[2:5] offset:1024
	s_add_u32 s44, s8, 0x2000
	s_addc_u32 s45, s9, 0
	s_add_u32 s46, s8, 0x4000
	s_addc_u32 s47, s9, 0
	s_add_u32 s48, s8, 0x6000
	s_addc_u32 s49, s9, 0
	s_add_u32 s50, s8, 0x8000
	s_addc_u32 s51, s9, 0
	s_add_u32 s52, s8, 0xa000
	s_addc_u32 s53, s9, 0
	s_add_u32 s54, s8, 0xc000
	s_addc_u32 s55, s9, 0
	s_add_u32 s56, s8, 0xe000
	s_addc_u32 s57, s9, 0
	s_add_u32 s58, s4, 0x2000
	s_addc_u32 s59, s5, 0
	s_add_u32 s60, s4, 0x4000
	s_addc_u32 s61, s5, 0
	s_add_u32 s62, s4, 0x6000
	s_addc_u32 s63, s5, 0
	s_add_u32 s64, s4, 0x8000
	s_addc_u32 s65, s5, 0
	s_add_u32 s66, s4, 0xa000
	s_addc_u32 s67, s5, 0
	s_add_u32 s68, s4, 0xc000
	s_addc_u32 s69, s5, 0
	s_add_u32 s70, s4, 0xe000
	s_addc_u32 s71, s5, 0
	s_add_u32 s72, s12, 0x2000
	s_addc_u32 s73, s13, 0
	s_add_u32 s74, s12, 0x3000
	s_addc_u32 s75, s13, 0
	s_add_u32 s76, s12, 0x9000
	s_addc_u32 s77, s13, 0
	s_add_u32 s78, s12, 0xb000
	s_addc_u32 s79, s13, 0
	s_add_u32 s80, s14, 0x2000
	s_addc_u32 s81, s15, 0
	s_add_u32 s82, s14, 0x3000
	s_addc_u32 s83, s15, 0
	s_add_u32 s84, s14, 0x9000
	s_addc_u32 s85, s15, 0
	s_add_u32 s86, s14, 0xb000
	s_addc_u32 s87, s15, 0
	s_branch .LBB3_142
